# grid barrier: member workgroups poll the top generation word directly (skip per-XCD relay), leader relay add not waited on
# baseline (speedup 1.0000x reference)
.LBB0_122:
	s_or_b64 exec, exec, s[2:3]
	v_readlane_b32 s2, v252, 17
	v_readlane_b32 s3, v252, 18
	s_waitcnt vmcnt(0)
	buffer_inv sc1
	s_nop 2
	global_atomic_add v1, v204, s[2:3]
.LBB0_123:
	s_or_b64 exec, exec, s[0:1]
	s_waitcnt lgkmcnt(0)
	s_barrier

.LBB0_163:
	v_readlane_b32 s2, v252, 15
	v_readlane_b32 s3, v252, 16
	v_cvt_f32_u32_e32 v0, v3
	v_sub_u32_e32 v5, 0, v3
	v_rcp_iflag_f32_e32 v0, v0
	s_nop 1
	global_atomic_add v4, v1, v204, s[2:3] sc0
	v_mul_f32_e32 v0, 0x4f7ffffe, v0
	v_cvt_u32_f32_e32 v0, v0
	v_mul_lo_u32 v5, v5, v0
	v_mul_hi_u32 v5, v0, v5
	v_add_u32_e32 v0, v0, v5
	s_waitcnt vmcnt(0)
	v_mul_hi_u32 v0, v4, v0
	v_mul_lo_u32 v5, v0, v3
	v_sub_u32_e32 v5, v4, v5
	v_add_u32_e32 v6, 1, v0
	v_cmp_ge_u32_e32 vcc, v5, v3
	v_add_u32_e32 v4, 1, v4
	s_nop 0
	v_cndmask_b32_e32 v0, v0, v6, vcc
	v_sub_u32_e32 v6, v5, v3
	v_cndmask_b32_e32 v5, v5, v6, vcc
	v_add_u32_e32 v6, 1, v0
	v_cmp_ge_u32_e32 vcc, v5, v3
	s_nop 1
	v_cndmask_b32_e32 v0, v0, v6, vcc
	v_mul_lo_u32 v5, v3, v0
	v_add_u32_e32 v3, v5, v3
	v_cmp_ne_u32_e32 vcc, v4, v3
	s_and_saveexec_b64 s[2:3], vcc
	s_xor_b64 s[2:3], exec, s[2:3]
	s_cbranch_execz .LBB0_177
	v_readlane_b32 s4, v252, 21
	v_readlane_b32 s5, v252, 22
	s_waitcnt lgkmcnt(0)
	s_nop 3
	global_load_dword v2, v1, s[4:5] sc1
	s_waitcnt vmcnt(0)
	v_cmp_eq_u32_e32 vcc, v2, v0
	s_and_saveexec_b64 s[4:5], vcc
	s_cbranch_execz .LBB0_176
	s_mov_b32 s17, 1
	s_mov_b64 s[6:7], 0
	s_branch .LBB0_167

.LBB0_194:
	s_or_b64 exec, exec, s[2:3]
	v_readlane_b32 s2, v252, 17
	v_readlane_b32 s3, v252, 18
	s_waitcnt vmcnt(0)
	buffer_inv sc1
	s_nop 2
	global_atomic_add v1, v204, s[2:3]
.LBB0_195:
	s_or_b64 exec, exec, s[0:1]
	s_waitcnt lgkmcnt(0)
	s_barrier

.LBB0_591:
	s_or_b64 exec, exec, s[2:3]
	v_readlane_b32 s2, v252, 17
	v_readlane_b32 s3, v252, 18
	s_waitcnt vmcnt(0)
	buffer_inv sc1
	s_nop 2
	global_atomic_add v1, v204, s[2:3]
.LBB0_592:
	s_or_b64 exec, exec, s[0:1]
	s_waitcnt lgkmcnt(0)
	s_barrier

.LBB0_717:
	s_or_b64 exec, exec, s[2:3]
	v_readlane_b32 s2, v252, 17
	v_readlane_b32 s3, v252, 18
	s_waitcnt vmcnt(0)
	buffer_inv sc1
	s_nop 2
	global_atomic_add v1, v204, s[2:3]
.LBB0_718:
	s_or_b64 exec, exec, s[0:1]
	s_waitcnt lgkmcnt(0)
	s_barrier

.LBB0_1196:
	s_or_b64 exec, exec, s[2:3]
	v_readlane_b32 s2, v252, 17
	v_readlane_b32 s3, v252, 18
	s_waitcnt vmcnt(0)
	buffer_inv sc1
	s_nop 2
	global_atomic_add v1, v204, s[2:3]
.LBB0_1197:
	s_or_b64 exec, exec, s[0:1]
	s_waitcnt lgkmcnt(0)
	s_barrier

.LBB0_1299:
	s_or_b64 exec, exec, s[2:3]
	v_readlane_b32 s2, v252, 17
	v_readlane_b32 s3, v252, 18
	s_waitcnt vmcnt(0)
	buffer_inv sc1
	s_nop 2
	global_atomic_add v1, v204, s[2:3]
.LBB0_1300:
	s_or_b64 exec, exec, s[0:1]
	s_waitcnt lgkmcnt(0)
	s_barrier

.LBB0_1378:
	s_or_b64 exec, exec, s[2:3]
	v_readlane_b32 s2, v252, 17
	v_readlane_b32 s3, v252, 18
	s_waitcnt vmcnt(0)
	buffer_inv sc1
	s_nop 2
	global_atomic_add v1, v204, s[2:3]
.LBB0_1379:
	s_or_b64 exec, exec, s[0:1]
	s_waitcnt lgkmcnt(0)
	s_barrier

.LBB0_1826:
	s_or_b64 exec, exec, s[2:3]
	v_readlane_b32 s2, v252, 17
	v_readlane_b32 s3, v252, 18
	s_waitcnt vmcnt(0)
	buffer_inv sc1
	s_nop 2
	global_atomic_add v1, v204, s[2:3]
.LBB0_1827:
	s_or_b64 exec, exec, s[0:1]
	s_waitcnt lgkmcnt(0)
	s_barrier

.LBB0_1925:
	s_or_b64 exec, exec, s[2:3]
	v_readlane_b32 s2, v252, 17
	v_readlane_b32 s3, v252, 18
	s_waitcnt vmcnt(0)
	buffer_inv sc1
	s_nop 2
	global_atomic_add v1, v204, s[2:3]
.LBB0_1926:
	s_or_b64 exec, exec, s[0:1]
	s_waitcnt lgkmcnt(0)
	s_barrier

.LBB0_2135:
	s_or_b64 exec, exec, s[2:3]
	v_readlane_b32 s2, v252, 17
	v_readlane_b32 s3, v252, 18
	s_waitcnt vmcnt(0)
	buffer_inv sc1
	s_nop 2
	global_atomic_add v1, v204, s[2:3]
.LBB0_2136:
	s_or_b64 exec, exec, s[0:1]
	s_waitcnt lgkmcnt(0)
	s_barrier

.LBB0_2180:
	v_readlane_b32 s2, v252, 15
	v_readlane_b32 s3, v252, 16
	v_cvt_f32_u32_e32 v0, v3
	v_sub_u32_e32 v5, 0, v3
	v_rcp_iflag_f32_e32 v0, v0
	s_nop 1
	global_atomic_add v4, v1, v204, s[2:3] sc0
	v_mul_f32_e32 v0, 0x4f7ffffe, v0
	v_cvt_u32_f32_e32 v0, v0
	v_mul_lo_u32 v5, v5, v0
	v_mul_hi_u32 v5, v0, v5
	v_add_u32_e32 v0, v0, v5
	s_waitcnt vmcnt(0)
	v_mul_hi_u32 v0, v4, v0
	v_mul_lo_u32 v5, v0, v3
	v_sub_u32_e32 v5, v4, v5
	v_add_u32_e32 v6, 1, v0
	v_cmp_ge_u32_e32 vcc, v5, v3
	v_add_u32_e32 v4, 1, v4
	s_nop 0
	v_cndmask_b32_e32 v0, v0, v6, vcc
	v_sub_u32_e32 v6, v5, v3
	v_cndmask_b32_e32 v5, v5, v6, vcc
	v_add_u32_e32 v6, 1, v0
	v_cmp_ge_u32_e32 vcc, v5, v3
	s_nop 1
	v_cndmask_b32_e32 v0, v0, v6, vcc
	v_mul_lo_u32 v5, v3, v0
	v_add_u32_e32 v3, v5, v3
	v_cmp_ne_u32_e32 vcc, v4, v3
	s_and_saveexec_b64 s[2:3], vcc
	s_xor_b64 s[2:3], exec, s[2:3]
	s_cbranch_execz .LBB0_2194
	v_readlane_b32 s4, v252, 21
	v_readlane_b32 s5, v252, 22
	s_waitcnt lgkmcnt(0)
	s_nop 3
	global_load_dword v2, v1, s[4:5] sc1
	s_waitcnt vmcnt(0)
	v_cmp_eq_u32_e32 vcc, v2, v0
	s_and_saveexec_b64 s[4:5], vcc
	s_cbranch_execz .LBB0_2193
	s_mov_b32 s16, 1
	s_mov_b64 s[6:7], 0
	s_branch .LBB0_2184
